# v20: v19 + the 8 packed fp32 multiplies between the MFMAs of the scan chunk step (state x decay, MFMA SrcC) split into scalar v_mul_f32
# baseline (speedup 1.0000x reference)
.LBB0_1734:
	s_mul_i32 s0, s69, 0x3300
	s_add_i32 s0, s74, s0
	s_add_i32 s1, s0, 0x2a00
	v_add_u32_e32 v18, s1, v185
	ds_read_b64_tr_b16 v[20:21], v18
	v_add3_u32 v18, s0, v186, v187
	ds_read2_b64 v[26:29], v18 offset1:4
	ds_read2_b64 v[30:33], v18 offset0:8 offset1:12
	v_add_u32_e32 v18, 0x800, v18
	v_cvt_pk_bf16_f32 v22, v2, v3
	v_cvt_pk_bf16_f32 v23, v4, v5
	v_cvt_pk_bf16_f32 v24, v10, v11
	v_cvt_pk_bf16_f32 v25, v12, v13
	ds_read2_b64 v[38:41], v18 offset0:32 offset1:36
	ds_read2_b64 v[42:45], v18 offset0:40 offset1:44
	s_waitcnt lgkmcnt(3)
	v_mfma_f32_16x16x32_bf16 v[26:29], v[26:29], v[22:25], 0
	s_waitcnt lgkmcnt(0)
	s_add_i32 s76, s69, s68
	v_cvt_pk_bf16_f32 v34, v6, v7
	v_cvt_pk_bf16_f32 v35, v8, v9
	v_cvt_pk_bf16_f32 v36, v14, v15
	v_cvt_pk_bf16_f32 v37, v16, v17
	s_waitcnt lgkmcnt(2)
	s_nop 0
	v_mfma_f32_16x16x32_bf16 v[26:29], v[30:33], v[34:37], v[26:29]
	s_nop 7
	v_cvt_pk_bf16_f32 v18, v26, v27
	v_add_u32_e32 v26, s0, v192
	ds_read_b128 v[30:33], v26 offset:8704
	v_add_u32_e32 v62, s0, v191
	ds_read_b128 v[46:49], v62 offset:12800
	v_cvt_pk_bf16_f32 v19, v28, v29
	ds_read_b128 v[26:29], v26 offset:9728
	ds_read_b128 v[50:53], v62 offset:12864
	v_add_u32_e32 v63, v62, v190
	ds_read_b128 v[54:57], v63 offset:4608
	ds_read_b128 v[58:61], v63 offset:5632
	s_waitcnt lgkmcnt(5)
	v_mfma_f32_16x16x32_bf16 v[30:33], v[30:33], v[18:21], 0
	s_waitcnt lgkmcnt(2)
	v_mul_f32_e32 v10, v10, v50
	v_mul_f32_e32 v11, v11, v51
	v_mul_f32_e32 v12, v12, v52
	v_mul_f32_e32 v13, v13, v53
	ds_read_b128 v[50:53], v63 offset:7680
	v_mfma_f32_16x16x32_bf16 v[22:25], v[38:41], v[22:25], 0
	s_nop 2
	v_cvt_pk_bf16_f32 v18, v30, v31
	v_cvt_pk_bf16_f32 v19, v32, v33
	ds_read_b128 v[30:33], v63 offset:6656
	v_mul_f32_e32 v2, v2, v46
	v_mul_f32_e32 v3, v3, v47
	v_mul_f32_e32 v4, v4, v48
	v_mul_f32_e32 v5, v5, v49
	ds_read_b128 v[46:49], v62 offset:12928
	v_mfma_f32_16x16x32_bf16 v[22:25], v[42:45], v[34:37], v[22:25]
	s_cmp_lt_u32 s76, 16
	s_waitcnt lgkmcnt(4)
	v_mfma_f32_16x16x32_bf16 v[2:5], v[54:57], v[18:21], v[2:5]
	ds_read_b128 v[54:57], v62 offset:12992
	s_waitcnt lgkmcnt(1)
	v_mul_f32_e32 v6, v6, v46
	v_mul_f32_e32 v7, v7, v47
	v_mul_f32_e32 v8, v8, v48
	v_mul_f32_e32 v9, v9, v49
	v_mfma_f32_16x16x32_bf16 v[10:13], v[58:61], v[18:21], v[10:13]
	s_waitcnt lgkmcnt(0)
	v_mul_f32_e32 v14, v14, v54
	v_mul_f32_e32 v15, v15, v55
	v_mul_f32_e32 v16, v16, v56
	v_mul_f32_e32 v17, v17, v57
	v_mfma_f32_16x16x32_bf16 v[6:9], v[30:33], v[18:21], v[6:9]
	s_nop 0
	v_mfma_f32_16x16x32_bf16 v[14:17], v[50:53], v[18:21], v[14:17]
	v_mfma_f32_16x16x32_bf16 v[18:21], v[26:29], v[18:21], v[22:25]
	s_cbranch_scc1 .LBB0_1731
	s_nop 6
	v_mov_b32_dpp v32, v18 quad_perm:[1,0,3,2] row_mask:0xf bank_mask:0xf bound_ctrl:1
	v_mov_b32_dpp v33, v19 quad_perm:[1,0,3,2] row_mask:0xf bank_mask:0xf bound_ctrl:1
	v_mov_b32_dpp v34, v20 quad_perm:[1,0,3,2] row_mask:0xf bank_mask:0xf bound_ctrl:1
	v_mov_b32_dpp v35, v21 quad_perm:[1,0,3,2] row_mask:0xf bank_mask:0xf bound_ctrl:1
	v_cndmask_b32_e64 v36, v18, v33, s[98:99]
	v_cndmask_b32_e64 v37, v32, v19, s[98:99]
	v_cndmask_b32_e64 v38, v20, v35, s[98:99]
	v_cndmask_b32_e64 v39, v34, v21, s[98:99]
	v_cvt_pk_bf16_f32 v36, v36, v37
	v_cvt_pk_bf16_f32 v38, v38, v39
	global_store_dword v[210:211], v36, off sc1
	global_store_dword v[212:213], v38, off sc1
	s_branch .LBB0_1731
